# P6 gate epilogue: eight gate loads per batch issued together (one wait), plus P7 epilogue batching and attention K-read hoist
# speedup vs baseline: 1.0129x; 1.0013x over previous
.LBB0_727:
	s_lshl_b32 s5, s29, 11
	s_ashr_i32 s8, s5, 31
	s_cmp_lt_i32 s29, 2
	s_cselect_b64 s[6:7], -1, 0
	s_cmp_gt_i32 s29, 1
	s_cselect_b64 s[30:31], -1, 0
	s_lshl_b32 s19, s4, 8
	s_add_u32 s4, s48, s5
	s_addc_u32 s5, s49, s8
	s_lshl_b32 s26, s28, 8
	s_ashr_i32 s27, s26, 31
	s_add_u32 s28, s4, s26
	s_addc_u32 s29, s5, s27
	v_add_u32_e32 v152, s19, v174
	v_mov_b64_e32 v[154:155], s[28:29]
	v_mad_i64_i32 v[154:155], s[4:5], v152, s60, v[154:155]
	v_lshl_add_u64 v[154:155], v[154:155], 0, v[142:143]
	global_load_dwordx2 v[166:167], v[154:155], off
	s_and_b64 vcc, exec, s[30:31]
	global_load_dwordx2 v[168:169], v[154:155], off offset:2048
.LBB0_729:
	global_load_dwordx2 v[162:163], v[154:155], off offset:128
	v_cndmask_b32_e64 v140, 0, 1, s[6:7]
	v_cmp_ne_u32_e64 s[8:9], 1, v140
	s_andn2_b64 vcc, exec, s[6:7]
	global_load_dwordx2 v[164:165], v[154:155], off offset:2176
.LBB0_731:
	v_or_b32_e32 v140, 16, v152
	v_mov_b64_e32 v[154:155], s[28:29]
	v_mad_i64_i32 v[154:155], s[4:5], v140, s60, v[154:155]
	v_lshl_add_u64 v[170:171], v[154:155], 0, v[142:143]
	global_load_dwordx2 v[158:159], v[170:171], off
	v_ashrrev_i32_e32 v153, 31, v152
	s_and_b64 vcc, exec, s[8:9]
	global_load_dwordx2 v[160:161], v[170:171], off offset:2048
.LBB0_733:
	global_load_dwordx2 v[154:155], v[170:171], off offset:128
	s_and_b64 vcc, exec, s[8:9]
	global_load_dwordx2 v[156:157], v[170:171], off offset:2176
.LBB0_735:
	s_waitcnt vmcnt(0)
	v_cvt_f32_ubyte0_e32 v140, v168
	v_max_f32_e32 v140, 1.0, v140
	v_rcp_f32_e32 v140, v140
	v_cvt_f32_ubyte1_e32 v170, v168
	v_max_f32_e32 v170, 1.0, v170
	v_rcp_f32_e32 v170, v170
	v_cvt_f32_ubyte2_e32 v171, v168
	v_lshlrev_b64 v[182:183], 12, v[152:153]
	v_cvt_f32_ubyte0_e32 v153, v166
	v_max_f32_e32 v171, 1.0, v171
	v_max_f32_e32 v153, 1.0, v153
	v_cndmask_b32_e64 v140, v180, v140, s[6:7]
	v_rcp_f32_e32 v171, v171
	v_mul_f32_e32 v140, v153, v140
	v_cvt_f32_ubyte1_e32 v153, v166
	v_max_f32_e32 v153, 1.0, v153
	v_cndmask_b32_e64 v170, v180, v170, s[6:7]
	v_mul_f32_e32 v153, v153, v170
	v_cvt_f32_ubyte2_e32 v170, v166
	v_cvt_f32_ubyte3_e32 v168, v168
	v_max_f32_e32 v170, 1.0, v170
	v_cndmask_b32_e64 v171, v180, v171, s[6:7]
	v_max_f32_e32 v168, 1.0, v168
	v_rcp_f32_e32 v168, v168
	v_mul_f32_e32 v171, v170, v171
	v_cvt_f32_ubyte0_e32 v170, v169
	v_max_f32_e32 v170, 1.0, v170
	v_cvt_f32_ubyte1_e32 v172, v169
	v_rcp_f32_e32 v170, v170
	v_max_f32_e32 v172, 1.0, v172
	v_cvt_f32_ubyte3_e32 v166, v166
	v_rcp_f32_e32 v172, v172
	v_max_f32_e32 v166, 1.0, v166
	v_cndmask_b32_e64 v168, v180, v168, s[6:7]
	v_mul_f32_e32 v166, v166, v168
	v_cvt_f32_ubyte0_e32 v168, v167
	v_max_f32_e32 v168, 1.0, v168
	v_cndmask_b32_e64 v170, v180, v170, s[6:7]
	v_mul_f32_e32 v173, v168, v170
	v_cndmask_b32_e64 v170, v180, v172, s[6:7]
	v_cvt_f32_ubyte2_e32 v172, v169
	v_max_f32_e32 v172, 1.0, v172
	v_cvt_f32_ubyte3_e32 v169, v169
	v_rcp_f32_e32 v172, v172
	v_max_f32_e32 v169, 1.0, v169
	v_cvt_f32_ubyte1_e32 v168, v167
	v_rcp_f32_e32 v169, v169
	v_max_f32_e32 v168, 1.0, v168
	v_mul_f32_e32 v181, v168, v170
	v_cvt_f32_ubyte2_e32 v168, v167
	v_max_f32_e32 v168, 1.0, v168
	v_cndmask_b32_e64 v170, v180, v172, s[6:7]
	v_cvt_f32_ubyte3_e32 v167, v167
	v_mul_f32_e32 v172, v168, v170
	v_max_f32_e32 v167, 1.0, v167
	v_cndmask_b32_e64 v168, v180, v169, s[6:7]
	v_mul_f32_e32 v167, v167, v168
	v_mul_f32_e32 v169, v92, v140
	v_mul_f32_e32 v170, v93, v153
	v_mul_f32_e32 v153, v94, v171
	v_mul_f32_e32 v168, v95, v166
	v_mul_f32_e32 v171, v90, v172
	v_mul_f32_e32 v172, v91, v167
	v_cndmask_b32_e64 v140, 0, 1, s[30:31]
	v_lshl_add_u64 v[166:167], s[12:13], 0, v[182:183]
	v_mul_f32_e32 v173, v88, v173
	v_mul_f32_e32 v181, v89, v181
	v_cmp_ne_u32_e64 s[4:5], 1, v140
	s_andn2_b64 vcc, exec, s[30:31]
	v_lshl_add_u64 v[166:167], s[26:27], 1, v[166:167]
	v_lshlrev_b32_e32 v140, 1, v142
	s_cbranch_vccnz .LBB0_737
	v_cvt_pk_bf16_f32 v182, v169, v170
	v_cvt_pk_bf16_f32 v183, v153, v168
	v_cvt_pk_bf16_f32 v184, v173, v181
	v_cvt_pk_bf16_f32 v185, v171, v172
	v_lshl_add_u64 v[168:169], v[166:167], 0, v[140:141]
	global_store_dwordx4 v[168:169], v[182:185], off
	s_branch .LBB0_738

.LBB0_747:
	v_add_u32_e32 v170, s19, v177
	v_mov_b64_e32 v[154:155], s[28:29]
	v_mad_i64_i32 v[154:155], s[30:31], v170, s60, v[154:155]
	v_lshl_add_u64 v[154:155], v[154:155], 0, v[142:143]
	global_load_dwordx2 v[166:167], v[154:155], off
	s_and_b64 vcc, exec, s[8:9]
	global_load_dwordx2 v[168:169], v[154:155], off offset:2048
.LBB0_749:
	global_load_dwordx2 v[162:163], v[154:155], off offset:128
	s_and_b64 vcc, exec, s[8:9]
	global_load_dwordx2 v[164:165], v[154:155], off offset:2176
.LBB0_751:
	v_or_b32_e32 v153, 16, v170
	v_mov_b64_e32 v[154:155], s[28:29]
	v_mad_i64_i32 v[154:155], s[30:31], v153, s60, v[154:155]
	v_lshl_add_u64 v[172:173], v[154:155], 0, v[142:143]
	global_load_dwordx2 v[158:159], v[172:173], off
	v_ashrrev_i32_e32 v171, 31, v170
	s_and_b64 vcc, exec, s[8:9]
	global_load_dwordx2 v[160:161], v[172:173], off offset:2048
.LBB0_753:
	global_load_dwordx2 v[154:155], v[172:173], off offset:128
	s_and_b64 vcc, exec, s[8:9]
	global_load_dwordx2 v[156:157], v[172:173], off offset:2176
.LBB0_755:
	s_waitcnt vmcnt(0)
	v_cvt_f32_ubyte0_e32 v153, v168
	v_max_f32_e32 v153, 1.0, v153
	v_rcp_f32_e32 v153, v153
	v_lshlrev_b64 v[182:183], 12, v[170:171]
	v_cvt_f32_ubyte1_e32 v171, v168
	v_max_f32_e32 v171, 1.0, v171
	v_rcp_f32_e32 v171, v171
	v_cvt_f32_ubyte2_e32 v172, v168
	v_cvt_f32_ubyte0_e32 v170, v166
	v_max_f32_e32 v172, 1.0, v172
	v_max_f32_e32 v170, 1.0, v170
	v_cndmask_b32_e64 v153, v180, v153, s[6:7]
	v_rcp_f32_e32 v172, v172
	v_mul_f32_e32 v153, v170, v153
	v_cvt_f32_ubyte1_e32 v170, v166
	v_max_f32_e32 v170, 1.0, v170
	v_cndmask_b32_e64 v171, v180, v171, s[6:7]
	v_mul_f32_e32 v170, v170, v171
	v_cvt_f32_ubyte2_e32 v171, v166
	v_cvt_f32_ubyte3_e32 v168, v168
	v_max_f32_e32 v171, 1.0, v171
	v_cndmask_b32_e64 v172, v180, v172, s[6:7]
	v_max_f32_e32 v168, 1.0, v168
	v_rcp_f32_e32 v168, v168
	v_mul_f32_e32 v171, v171, v172
	v_cvt_f32_ubyte0_e32 v172, v169
	v_max_f32_e32 v172, 1.0, v172
	v_rcp_f32_e32 v172, v172
	v_cvt_f32_ubyte1_e32 v173, v169
	v_cvt_f32_ubyte3_e32 v166, v166
	v_max_f32_e32 v173, 1.0, v173
	v_max_f32_e32 v166, 1.0, v166
	v_cndmask_b32_e64 v168, v180, v168, s[6:7]
	v_rcp_f32_e32 v173, v173
	v_cvt_f32_ubyte2_e32 v181, v169
	v_mul_f32_e32 v166, v166, v168
	v_cvt_f32_ubyte0_e32 v168, v167
	v_max_f32_e32 v181, 1.0, v181
	v_cvt_f32_ubyte3_e32 v169, v169
	v_max_f32_e32 v168, 1.0, v168
	v_cndmask_b32_e64 v172, v180, v172, s[6:7]
	v_rcp_f32_e32 v181, v181
	v_max_f32_e32 v169, 1.0, v169
	v_mul_f32_e32 v172, v168, v172
	v_cvt_f32_ubyte1_e32 v168, v167
	v_rcp_f32_e32 v169, v169
	v_max_f32_e32 v168, 1.0, v168
	v_cndmask_b32_e64 v173, v180, v173, s[6:7]
	v_mul_f32_e32 v184, v168, v173
	v_cvt_f32_ubyte2_e32 v168, v167
	v_max_f32_e32 v168, 1.0, v168
	v_cndmask_b32_e64 v173, v180, v181, s[6:7]
	v_cvt_f32_ubyte3_e32 v167, v167
	v_mul_f32_e32 v185, v168, v173
	v_max_f32_e32 v167, 1.0, v167
	v_cndmask_b32_e64 v168, v180, v169, s[6:7]
	v_mul_f32_e32 v167, v167, v168
	v_mul_f32_e32 v168, v79, v166
	v_mul_f32_e32 v173, v72, v172
	v_mul_f32_e32 v172, v75, v167
	v_lshl_add_u64 v[166:167], s[12:13], 0, v[182:183]
	v_mul_f32_e32 v169, v76, v153
	v_mul_f32_e32 v170, v77, v170
	v_mul_f32_e32 v153, v78, v171
	v_mul_f32_e32 v181, v73, v184
	v_mul_f32_e32 v171, v74, v185
	s_and_b64 vcc, exec, s[4:5]
	v_lshl_add_u64 v[166:167], s[26:27], 1, v[166:167]
	s_cbranch_vccnz .LBB0_757
	v_cvt_pk_bf16_f32 v182, v169, v170
	v_cvt_pk_bf16_f32 v183, v153, v168
	v_cvt_pk_bf16_f32 v184, v173, v181
	v_cvt_pk_bf16_f32 v185, v171, v172
	v_lshl_add_u64 v[168:169], v[166:167], 0, v[140:141]
	global_store_dwordx4 v[168:169], v[182:185], off
	s_branch .LBB0_758

.LBB0_767:
	v_add_u32_e32 v170, 0x80, v152
	v_mov_b64_e32 v[154:155], s[28:29]
	v_mad_i64_i32 v[154:155], s[30:31], v170, s60, v[154:155]
	v_lshl_add_u64 v[154:155], v[154:155], 0, v[142:143]
	global_load_dwordx2 v[166:167], v[154:155], off
	s_and_b64 vcc, exec, s[8:9]
	global_load_dwordx2 v[168:169], v[154:155], off offset:2048

.LBB0_775:
	s_waitcnt vmcnt(0)
	v_cvt_f32_ubyte0_e32 v153, v168
	v_max_f32_e32 v153, 1.0, v153
	v_rcp_f32_e32 v153, v153
	v_lshlrev_b64 v[182:183], 12, v[170:171]
	v_cvt_f32_ubyte1_e32 v171, v168
	v_max_f32_e32 v171, 1.0, v171
	v_rcp_f32_e32 v171, v171
	v_cvt_f32_ubyte2_e32 v172, v168
	v_cvt_f32_ubyte0_e32 v170, v166
	v_max_f32_e32 v172, 1.0, v172
	v_max_f32_e32 v170, 1.0, v170
	v_cndmask_b32_e64 v153, v180, v153, s[6:7]
	v_rcp_f32_e32 v172, v172
	v_mul_f32_e32 v153, v170, v153
	v_cvt_f32_ubyte1_e32 v170, v166
	v_max_f32_e32 v170, 1.0, v170
	v_cndmask_b32_e64 v171, v180, v171, s[6:7]
	v_mul_f32_e32 v170, v170, v171
	v_cvt_f32_ubyte2_e32 v171, v166
	v_cvt_f32_ubyte3_e32 v168, v168
	v_max_f32_e32 v171, 1.0, v171
	v_cndmask_b32_e64 v172, v180, v172, s[6:7]
	v_max_f32_e32 v168, 1.0, v168
	v_rcp_f32_e32 v168, v168
	v_mul_f32_e32 v171, v171, v172
	v_cvt_f32_ubyte0_e32 v172, v169
	v_max_f32_e32 v172, 1.0, v172
	v_rcp_f32_e32 v172, v172
	v_cvt_f32_ubyte1_e32 v173, v169
	v_cvt_f32_ubyte3_e32 v166, v166
	v_max_f32_e32 v173, 1.0, v173
	v_max_f32_e32 v166, 1.0, v166
	v_cndmask_b32_e64 v168, v180, v168, s[6:7]
	v_rcp_f32_e32 v173, v173
	v_cvt_f32_ubyte2_e32 v181, v169
	v_mul_f32_e32 v166, v166, v168
	v_cvt_f32_ubyte0_e32 v168, v167
	v_max_f32_e32 v181, 1.0, v181
	v_cvt_f32_ubyte3_e32 v169, v169
	v_max_f32_e32 v168, 1.0, v168
	v_cndmask_b32_e64 v172, v180, v172, s[6:7]
	v_rcp_f32_e32 v181, v181
	v_max_f32_e32 v169, 1.0, v169
	v_mul_f32_e32 v172, v168, v172
	v_cvt_f32_ubyte1_e32 v168, v167
	v_rcp_f32_e32 v169, v169
	v_max_f32_e32 v168, 1.0, v168
	v_cndmask_b32_e64 v173, v180, v173, s[6:7]
	v_mul_f32_e32 v184, v168, v173
	v_cvt_f32_ubyte2_e32 v168, v167
	v_max_f32_e32 v168, 1.0, v168
	v_cndmask_b32_e64 v173, v180, v181, s[6:7]
	v_cvt_f32_ubyte3_e32 v167, v167
	v_mul_f32_e32 v185, v168, v173
	v_max_f32_e32 v167, 1.0, v167
	v_cndmask_b32_e64 v168, v180, v169, s[6:7]
	v_mul_f32_e32 v167, v167, v168
	v_mul_f32_e32 v168, v31, v166
	v_mul_f32_e32 v173, v24, v172
	v_mul_f32_e32 v172, v27, v167
	v_lshl_add_u64 v[166:167], s[12:13], 0, v[182:183]
	v_mul_f32_e32 v169, v28, v153
	v_mul_f32_e32 v170, v29, v170
	v_mul_f32_e32 v153, v30, v171
	v_mul_f32_e32 v181, v25, v184
	v_mul_f32_e32 v171, v26, v185
	s_and_b64 vcc, exec, s[4:5]
	v_lshl_add_u64 v[166:167], s[26:27], 1, v[166:167]
	s_cbranch_vccnz .LBB0_777
	v_cvt_pk_bf16_f32 v182, v169, v170
	v_cvt_pk_bf16_f32 v183, v153, v168
	v_cvt_pk_bf16_f32 v184, v173, v181
	v_cvt_pk_bf16_f32 v185, v171, v172
	v_lshl_add_u64 v[168:169], v[166:167], 0, v[140:141]
	global_store_dwordx4 v[168:169], v[182:185], off
	s_branch .LBB0_778

.LBB0_787:
	v_add_u32_e32 v170, 0xa0, v152
	v_mov_b64_e32 v[154:155], s[28:29]
	v_mad_i64_i32 v[154:155], s[30:31], v170, s60, v[154:155]
	v_lshl_add_u64 v[154:155], v[154:155], 0, v[142:143]
	global_load_dwordx2 v[166:167], v[154:155], off
	s_and_b64 vcc, exec, s[8:9]
	global_load_dwordx2 v[168:169], v[154:155], off offset:2048

.LBB0_791:
	v_or_b32_e32 v153, 16, v170
	v_mov_b64_e32 v[154:155], s[28:29]
	v_mad_i64_i32 v[154:155], s[28:29], v153, s60, v[154:155]
	v_lshl_add_u64 v[172:173], v[154:155], 0, v[142:143]
	global_load_dwordx2 v[158:159], v[172:173], off
	v_ashrrev_i32_e32 v171, 31, v170
	s_and_b64 vcc, exec, s[8:9]
	global_load_dwordx2 v[160:161], v[172:173], off offset:2048

.LBB0_795:
	s_waitcnt vmcnt(0)
	v_cvt_f32_ubyte0_e32 v153, v168
	v_max_f32_e32 v153, 1.0, v153
	v_rcp_f32_e32 v153, v153
	v_lshlrev_b64 v[182:183], 12, v[170:171]
	v_cvt_f32_ubyte1_e32 v171, v168
	v_max_f32_e32 v171, 1.0, v171
	v_rcp_f32_e32 v171, v171
	v_cvt_f32_ubyte2_e32 v172, v168
	v_cvt_f32_ubyte0_e32 v170, v166
	v_max_f32_e32 v172, 1.0, v172
	v_max_f32_e32 v170, 1.0, v170
	v_cndmask_b32_e64 v153, v180, v153, s[6:7]
	v_rcp_f32_e32 v172, v172
	v_mul_f32_e32 v153, v170, v153
	v_cvt_f32_ubyte1_e32 v170, v166
	v_max_f32_e32 v170, 1.0, v170
	v_cndmask_b32_e64 v171, v180, v171, s[6:7]
	v_mul_f32_e32 v170, v170, v171
	v_cvt_f32_ubyte2_e32 v171, v166
	v_cvt_f32_ubyte3_e32 v168, v168
	v_max_f32_e32 v171, 1.0, v171
	v_cndmask_b32_e64 v172, v180, v172, s[6:7]
	v_max_f32_e32 v168, 1.0, v168
	v_rcp_f32_e32 v168, v168
	v_mul_f32_e32 v171, v171, v172
	v_cvt_f32_ubyte0_e32 v172, v169
	v_max_f32_e32 v172, 1.0, v172
	v_rcp_f32_e32 v172, v172
	v_cvt_f32_ubyte1_e32 v173, v169
	v_cvt_f32_ubyte3_e32 v166, v166
	v_max_f32_e32 v173, 1.0, v173
	v_max_f32_e32 v166, 1.0, v166
	v_cndmask_b32_e64 v168, v180, v168, s[6:7]
	v_rcp_f32_e32 v173, v173
	v_cvt_f32_ubyte2_e32 v181, v169
	v_mul_f32_e32 v166, v166, v168
	v_cvt_f32_ubyte0_e32 v168, v167
	v_max_f32_e32 v181, 1.0, v181
	v_cvt_f32_ubyte3_e32 v169, v169
	v_max_f32_e32 v168, 1.0, v168
	v_cndmask_b32_e64 v172, v180, v172, s[6:7]
	v_rcp_f32_e32 v181, v181
	v_max_f32_e32 v169, 1.0, v169
	v_mul_f32_e32 v172, v168, v172
	v_cvt_f32_ubyte1_e32 v168, v167
	v_rcp_f32_e32 v169, v169
	v_max_f32_e32 v168, 1.0, v168
	v_cndmask_b32_e64 v173, v180, v173, s[6:7]
	v_mul_f32_e32 v184, v168, v173
	v_cvt_f32_ubyte2_e32 v168, v167
	v_max_f32_e32 v168, 1.0, v168
	v_cndmask_b32_e64 v173, v180, v181, s[6:7]
	v_cvt_f32_ubyte3_e32 v167, v167
	v_mul_f32_e32 v185, v168, v173
	v_max_f32_e32 v167, 1.0, v167
	v_cndmask_b32_e64 v168, v180, v169, s[6:7]
	v_mul_f32_e32 v167, v167, v168
	v_mul_f32_e32 v168, v15, v166
	v_mul_f32_e32 v173, v8, v172
	v_mul_f32_e32 v172, v11, v167
	v_lshl_add_u64 v[166:167], s[12:13], 0, v[182:183]
	v_mul_f32_e32 v169, v12, v153
	v_mul_f32_e32 v170, v13, v170
	v_mul_f32_e32 v153, v14, v171
	v_mul_f32_e32 v181, v9, v184
	v_mul_f32_e32 v171, v10, v185
	s_and_b64 vcc, exec, s[4:5]
	v_lshl_add_u64 v[166:167], s[26:27], 1, v[166:167]
	s_cbranch_vccnz .LBB0_797
	v_cvt_pk_bf16_f32 v182, v169, v170
	v_cvt_pk_bf16_f32 v183, v153, v168
	v_cvt_pk_bf16_f32 v184, v173, v181
	v_cvt_pk_bf16_f32 v185, v171, v172
	v_lshl_add_u64 v[168:169], v[166:167], 0, v[140:141]
	global_store_dwordx4 v[168:169], v[182:185], off
	s_branch .LBB0_798
